# rope transposed stores: quad lane order changed to (fq0,fq2,fq1,fq3) so adjacent lanes hold contiguous 32-B pairs
# speedup vs baseline: 1.0138x; 1.0000x over previous
; #define PG8_ST8(rs, b0, p, v) __builtin_amdgcn_raw_buffer_store_b64(v, rs, (int)((const char*)(p) - (const char*)(b0)), 0, 16)
; __device__ __forceinline__ unsigned cvt_pk_bf16(float lo, float hi) { unsigned r; asm volatile("v_cvt_pk_bf16_f32 %0, %1, %2" : "=v"(r) : "v"(lo), "v"(hi)); return r; }
;     __device__ __forceinline__ void operator()(const f32x4 (&acc)[2][2][4][2], const Unit& u, int wr, int wc, int fr, int fq) const {
;     ...
;             const float sc = (pn <= 6 || (pn >= 9 && pn <= 11)) ? qscale : 1.0f;
;             const int f = 16 * (wc & 1) + 4 * fq, col0 = pn * BM + 64 * (wc >> 1) + f;
; #pragma unroll
;             for (int ai = 0; ai < 2; ++ai) {
;                 f32x4 c4[4], s4[4];
; #pragma unroll
;                 for (int m = 0; m < 4; ++m) { const int row = row0 + ai * HALF + m * 16; c4[m] = *(const f32x4*)(rc + (size_t)row * 32 + f); s4[m] = *(const f32x4*)(rs + (size_t)row * 32 + f); }
;                 asm volatile("" ::: "memory");
; #pragma unroll
;                 for (int m = 0; m < 4; ++m) { const int row = row0 + ai * HALF + m * 16;
;                     const f32x4 cc = c4[m] * sc, ss = s4[m] * sc;
;                     bf16_t* rowp = P + (size_t)row * ldp + col0;
; #pragma unroll
;                     for (int bj = 0; bj < 2; ++bj) { const f32x4 x1 = acc[ai][bj][m][0], x2 = acc[ai][bj][m][1]; const f32x4 o1 = x1 * cc - x2 * ss, o2 = x2 * cc + x1 * ss;
;                         u32x2 w1, w2; w1.x = cvt_pk_bf16(o1[0], o1[1]); w1.y = cvt_pk_bf16(o1[2], o1[3]); w2.x = cvt_pk_bf16(o2[0], o2[1]); w2.y = cvt_pk_bf16(o2[2], o2[3]);
;                         PG8_ST8(rsp_, P, rowp + bj * HALF, w1); PG8_ST8(rsp_, P, rowp + bj * HALF + 32, w2); } }
.LBB0_230:
	v_lshl_add_u32 v164, s27, 8, v175
	s_add_i32 s27, s62, s56
	s_cmp_gt_i32 s27, 3
	s_mov_b64 s[34:35], -1
	s_cbranch_scc0 .LBB0_237
	s_cmp_lg_u32 s27, 8
	s_cselect_b64 s[34:35], -1, 0
	s_cmp_lt_u32 s27, 15
	s_cselect_b64 s[36:37], -1, 0
	s_and_b64 s[36:37], s[34:35], s[36:37]
	s_mov_b64 s[34:35], -1
	s_and_b64 vcc, exec, s[36:37]
	v_add_u32_e32 v172, 0x80, v164
	v_add_u32_e32 v170, 0x90, v164
	v_add_u32_e32 v168, 0xa0, v164
	v_add_u32_e32 v166, 0xb0, v164
	s_cbranch_vccz .LBB0_233
	s_cmp_lt_u32 s27, 7
	s_cselect_b64 s[34:35], -1, 0
	s_add_i32 s36, s27, -9
	s_cmp_lt_u32 s36, 3
	s_cselect_b64 s[36:37], -1, 0
	s_or_b64 vcc, s[34:35], s[36:37]
	v_mov_b32_e32 v132, 0x3e38aa3b
	v_ashrrev_i32_e32 v165, 31, v164
	v_cndmask_b32_e32 v174, 1.0, v132, vcc
	v_lshlrev_b64 v[132:133], 7, v[164:165]
	v_lshl_add_u64 v[134:135], v[154:155], 0, v[132:133]
	v_lshl_add_u64 v[132:133], v[156:157], 0, v[132:133]
	global_load_dwordx4 v[176:179], v[134:135], off
	global_load_dwordx4 v[184:187], v[132:133], off
	v_or_b32_e32 v192, 16, v164
	v_ashrrev_i32_e32 v193, 31, v192
	v_lshlrev_b64 v[132:133], 7, v[192:193]
	v_lshl_add_u64 v[134:135], v[154:155], 0, v[132:133]
	v_lshl_add_u64 v[132:133], v[156:157], 0, v[132:133]
	global_load_dwordx4 v[188:191], v[134:135], off
	global_load_dwordx4 v[218:221], v[132:133], off
	v_or_b32_e32 v182, 32, v164
	v_ashrrev_i32_e32 v183, 31, v182
	v_lshlrev_b64 v[132:133], 7, v[182:183]
	v_lshl_add_u64 v[134:135], v[154:155], 0, v[132:133]
	v_lshl_add_u64 v[132:133], v[156:157], 0, v[132:133]
	global_load_dwordx4 v[144:147], v[134:135], off
	global_load_dwordx4 v[140:143], v[132:133], off
	v_or_b32_e32 v180, 48, v164
	v_ashrrev_i32_e32 v181, 31, v180
	v_lshlrev_b64 v[132:133], 7, v[180:181]
	v_lshl_add_u64 v[134:135], v[154:155], 0, v[132:133]
	v_lshl_add_u64 v[132:133], v[156:157], 0, v[132:133]
	global_load_dwordx4 v[136:139], v[134:135], off
	s_movk_i32 s36, 0x2400
	global_load_dwordx4 v[132:135], v[132:133], off
	v_ashrrev_i32_e32 v173, 31, v172
	v_ashrrev_i32_e32 v171, 31, v170
	v_ashrrev_i32_e32 v169, 31, v168
	v_ashrrev_i32_e32 v167, 31, v166
	s_waitcnt vmcnt(0)
	v_pk_mul_f32 v[198:199], v[174:175], v[178:179] op_sel_hi:[0,1]
	v_pk_mul_f32 v[186:187], v[174:175], v[186:187] op_sel_hi:[0,1]
	v_pk_mul_f32 v[184:185], v[174:175], v[184:185] op_sel_hi:[0,1]
	v_pk_mul_f32 v[200:201], v[174:175], v[176:177] op_sel_hi:[0,1]
	v_mov_b64_e32 v[176:177], s[20:21]
	v_lshrrev_b32_e32 v245, 2, v215
	v_and_b32_e32 v246, 15, v215
	v_sub_u32_e32 v245, v245, v246
	v_mad_i64_i32 v[176:177], s[34:35], v245, s36, v[176:177]
	v_pk_mul_f32 v[208:209], v[118:119], v[186:187]
	v_pk_mul_f32 v[222:223], v[116:117], v[184:185]
	v_mad_i64_i32 v[206:207], s[34:35], v164, s36, v[176:177]
	v_lshl_or_b32 v178, s27, 9, v202
	v_mov_b32_e32 v179, v2
	v_bfe_u32 v244, v215, 1, 1
	v_and_b32_e32 v246, 1, v215
	v_lshl_or_b32 v244, v246, 1, v244
	v_lshrrev_b32_e32 v246, 4, v215
	v_sub_u32_e32 v246, v244, v246
	v_lshl_add_u32 v178, v246, 3, v178
	v_and_b32_e32 v246, 1, v244
	v_mad_u32_u24 v178, v246, 56, v178
	v_and_b32_e32 v246, 60, v215
	v_lshl_or_b32 v244, v244, 6, v246
	v_pk_fma_f32 v[208:209], v[126:127], v[198:199], v[208:209] neg_lo:[0,0,1] neg_hi:[0,0,1]
	v_pk_fma_f32 v[222:223], v[124:125], v[200:201], v[222:223] neg_lo:[0,0,1] neg_hi:[0,0,1]
	v_pk_mul_f32 v[224:225], v[126:127], v[186:187]
	v_pk_mul_f32 v[226:227], v[124:125], v[184:185]
	v_lshl_add_u64 v[206:207], v[206:207], 0, v[178:179]
	v_pk_fma_f32 v[224:225], v[118:119], v[198:199], v[224:225]
	v_pk_fma_f32 v[226:227], v[116:117], v[200:201], v[226:227]
	v_cvt_pk_bf16_f32 v222, v222, v223
	v_cvt_pk_bf16_f32 v223, v208, v209
	v_mad_i64_i32 v[192:193], s[34:35], v192, s36, v[176:177]
	v_cvt_pk_bf16_f32 v208, v226, v227
	v_cvt_pk_bf16_f32 v209, v224, v225
	v_mov_b32_e32 v228, v222
	v_mov_b32_e32 v229, v223
	v_mov_b32_e32 v230, v208
	v_mov_b32_e32 v231, v209
	s_nop 1
	v_permlane16_swap_b32_e32 v228, v230
	v_permlane16_swap_b32_e32 v229, v231
	ds_bpermute_b32 v228, v244, v228
	ds_bpermute_b32 v229, v244, v229
	ds_bpermute_b32 v230, v244, v230
	ds_bpermute_b32 v231, v244, v231
	v_pk_mul_f32 v[208:209], v[122:123], v[186:187]
	v_pk_mul_f32 v[222:223], v[120:121], v[184:185]
	v_pk_mul_f32 v[186:187], v[130:131], v[186:187]
	v_pk_mul_f32 v[184:185], v[128:129], v[184:185]
	v_pk_fma_f32 v[186:187], v[122:123], v[198:199], v[186:187]
	v_pk_fma_f32 v[184:185], v[120:121], v[200:201], v[184:185]
	v_pk_fma_f32 v[208:209], v[130:131], v[198:199], v[208:209] neg_lo:[0,0,1] neg_hi:[0,0,1]
	v_pk_fma_f32 v[222:223], v[128:129], v[200:201], v[222:223] neg_lo:[0,0,1] neg_hi:[0,0,1]
	v_lshl_add_u64 v[192:193], v[192:193], 0, v[178:179]
	v_cvt_pk_bf16_f32 v198, v222, v223
	v_cvt_pk_bf16_f32 v199, v208, v209
	v_cvt_pk_bf16_f32 v184, v184, v185
	v_cvt_pk_bf16_f32 v185, v186, v187
	v_pk_mul_f32 v[186:187], v[174:175], v[190:191] op_sel_hi:[0,1]
	v_pk_mul_f32 v[190:191], v[174:175], v[218:219] op_sel_hi:[0,1]
	v_mov_b32_e32 v232, v198
	v_mov_b32_e32 v233, v199
	v_mov_b32_e32 v234, v184
	v_mov_b32_e32 v235, v185
	s_nop 1
	v_permlane16_swap_b32_e32 v232, v234
	v_permlane16_swap_b32_e32 v233, v235
	ds_bpermute_b32 v232, v244, v232
	ds_bpermute_b32 v233, v244, v233
	ds_bpermute_b32 v234, v244, v234
	ds_bpermute_b32 v235, v244, v235
	s_waitcnt lgkmcnt(4)
; #define PG8_ST8(rs, b0, p, v) __builtin_amdgcn_raw_buffer_store_b64(v, rs, (int)((const char*)(p) - (const char*)(b0)), 0, 16)
; __device__ __forceinline__ unsigned cvt_pk_bf16(float lo, float hi) { unsigned r; asm volatile("v_cvt_pk_bf16_f32 %0, %1, %2" : "=v"(r) : "v"(lo), "v"(hi)); return r; }
;     __device__ __forceinline__ void operator()(const f32x4 (&acc)[2][2][4][2], const Unit& u, int wr, int wc, int fr, int fq) const {
;     ...
;                 for (int m = 0; m < 4; ++m) { const int row = row0 + ai * HALF + m * 16;
;                     const f32x4 cc = c4[m] * sc, ss = s4[m] * sc;
;                     bf16_t* rowp = P + (size_t)row * ldp + col0;
; #pragma unroll
;                     for (int bj = 0; bj < 2; ++bj) { const f32x4 x1 = acc[ai][bj][m][0], x2 = acc[ai][bj][m][1]; const f32x4 o1 = x1 * cc - x2 * ss, o2 = x2 * cc + x1 * ss;
;                         u32x2 w1, w2; w1.x = cvt_pk_bf16(o1[0], o1[1]); w1.y = cvt_pk_bf16(o1[2], o1[3]); w2.x = cvt_pk_bf16(o2[0], o2[1]); w2.y = cvt_pk_bf16(o2[2], o2[3]);
;                         PG8_ST8(rsp_, P, rowp + bj * HALF, w1); PG8_ST8(rsp_, P, rowp + bj * HALF + 32, w2); } }
	global_store_dwordx4 v[206:207], v[228:231], off
	v_pk_mul_f32 v[184:185], v[174:175], v[188:189] op_sel_hi:[0,1]
	v_pk_mul_f32 v[188:189], v[174:175], v[220:221] op_sel_hi:[0,1]
	v_pk_mul_f32 v[198:199], v[100:101], v[190:191]
	v_pk_mul_f32 v[200:201], v[102:103], v[188:189]
	v_pk_fma_f32 v[198:199], v[108:109], v[184:185], v[198:199] neg_lo:[0,0,1] neg_hi:[0,0,1]
	v_pk_fma_f32 v[200:201], v[110:111], v[186:187], v[200:201] neg_lo:[0,0,1] neg_hi:[0,0,1]
	v_pk_mul_f32 v[204:205], v[108:109], v[190:191]
	v_pk_mul_f32 v[208:209], v[110:111], v[188:189]
	v_cvt_pk_bf16_f32 v198, v198, v199
	v_cvt_pk_bf16_f32 v199, v200, v201
	v_pk_fma_f32 v[204:205], v[100:101], v[184:185], v[204:205]
	v_pk_fma_f32 v[208:209], v[102:103], v[186:187], v[208:209]
	v_cvt_pk_bf16_f32 v200, v204, v205
	v_pk_mul_f32 v[142:143], v[174:175], v[142:143] op_sel_hi:[0,1]
	v_cvt_pk_bf16_f32 v201, v208, v209
	v_mov_b32_e32 v236, v198
	v_mov_b32_e32 v237, v199
	v_mov_b32_e32 v238, v200
	v_mov_b32_e32 v239, v201
	s_nop 1
	v_permlane16_swap_b32_e32 v236, v238
	v_permlane16_swap_b32_e32 v237, v239
	ds_bpermute_b32 v236, v244, v236
	ds_bpermute_b32 v237, v244, v237
	ds_bpermute_b32 v238, v244, v238
	ds_bpermute_b32 v239, v244, v239
	s_waitcnt lgkmcnt(4)
	global_store_dwordx4 v[206:207], v[232:235], off offset:256
	v_pk_mul_f32 v[198:199], v[104:105], v[190:191]
	v_pk_mul_f32 v[190:191], v[112:113], v[190:191]
	v_pk_mul_f32 v[200:201], v[106:107], v[188:189]
	v_pk_fma_f32 v[198:199], v[112:113], v[184:185], v[198:199] neg_lo:[0,0,1] neg_hi:[0,0,1]
	v_pk_mul_f32 v[188:189], v[114:115], v[188:189]
	v_pk_fma_f32 v[184:185], v[104:105], v[184:185], v[190:191]
	v_pk_fma_f32 v[200:201], v[114:115], v[186:187], v[200:201] neg_lo:[0,0,1] neg_hi:[0,0,1]
	v_pk_fma_f32 v[186:187], v[106:107], v[186:187], v[188:189]
	v_cvt_pk_bf16_f32 v188, v198, v199
	v_cvt_pk_bf16_f32 v189, v200, v201
	v_cvt_pk_bf16_f32 v184, v184, v185
	v_pk_mul_f32 v[140:141], v[174:175], v[140:141] op_sel_hi:[0,1]
	v_cvt_pk_bf16_f32 v185, v186, v187
	v_mov_b32_e32 v240, v188
	v_mov_b32_e32 v241, v189
	v_mov_b32_e32 v242, v184
	v_mov_b32_e32 v243, v185
	s_nop 1
	v_permlane16_swap_b32_e32 v240, v242
	v_permlane16_swap_b32_e32 v241, v243
	ds_bpermute_b32 v240, v244, v240
	ds_bpermute_b32 v241, v244, v241
	ds_bpermute_b32 v242, v244, v242
	ds_bpermute_b32 v243, v244, v243
	s_waitcnt lgkmcnt(4)
	global_store_dwordx4 v[192:193], v[236:239], off
	v_pk_mul_f32 v[144:145], v[174:175], v[144:145] op_sel_hi:[0,1]
	v_pk_mul_f32 v[146:147], v[174:175], v[146:147] op_sel_hi:[0,1]
	v_pk_mul_f32 v[184:185], v[84:85], v[140:141]
	v_pk_mul_f32 v[186:187], v[86:87], v[142:143]
	v_mad_i64_i32 v[182:183], s[34:35], v182, s36, v[176:177]
	v_pk_fma_f32 v[186:187], v[94:95], v[146:147], v[186:187] neg_lo:[0,0,1] neg_hi:[0,0,1]
	v_pk_fma_f32 v[184:185], v[92:93], v[144:145], v[184:185] neg_lo:[0,0,1] neg_hi:[0,0,1]
	v_pk_mul_f32 v[188:189], v[92:93], v[140:141]
	v_pk_mul_f32 v[190:191], v[94:95], v[142:143]
	v_lshl_add_u64 v[182:183], v[182:183], 0, v[178:179]
	v_pk_fma_f32 v[190:191], v[86:87], v[146:147], v[190:191]
	v_pk_fma_f32 v[188:189], v[84:85], v[144:145], v[188:189]
	v_cvt_pk_bf16_f32 v184, v184, v185
	v_cvt_pk_bf16_f32 v185, v186, v187
	v_pk_mul_f32 v[134:135], v[174:175], v[134:135] op_sel_hi:[0,1]
	v_cvt_pk_bf16_f32 v186, v188, v189
	v_cvt_pk_bf16_f32 v187, v190, v191
	v_mov_b32_e32 v228, v184
	v_mov_b32_e32 v229, v185
	v_mov_b32_e32 v230, v186
	v_mov_b32_e32 v231, v187
	s_nop 1
	v_permlane16_swap_b32_e32 v228, v230
	v_permlane16_swap_b32_e32 v229, v231
	ds_bpermute_b32 v228, v244, v228
	ds_bpermute_b32 v229, v244, v229
	ds_bpermute_b32 v230, v244, v230
	ds_bpermute_b32 v231, v244, v231
	s_waitcnt lgkmcnt(4)
	global_store_dwordx4 v[192:193], v[240:243], off offset:256
	v_pk_mul_f32 v[184:185], v[88:89], v[140:141]
	v_pk_mul_f32 v[186:187], v[90:91], v[142:143]
	v_pk_mul_f32 v[140:141], v[96:97], v[140:141]
	v_pk_mul_f32 v[142:143], v[98:99], v[142:143]
	v_pk_fma_f32 v[186:187], v[98:99], v[146:147], v[186:187] neg_lo:[0,0,1] neg_hi:[0,0,1]
	v_pk_fma_f32 v[184:185], v[96:97], v[144:145], v[184:185] neg_lo:[0,0,1] neg_hi:[0,0,1]
	v_pk_fma_f32 v[142:143], v[90:91], v[146:147], v[142:143]
	v_pk_fma_f32 v[140:141], v[88:89], v[144:145], v[140:141]
	v_cvt_pk_bf16_f32 v144, v184, v185
	v_cvt_pk_bf16_f32 v145, v186, v187
	v_pk_mul_f32 v[132:133], v[174:175], v[132:133] op_sel_hi:[0,1]
	v_cvt_pk_bf16_f32 v140, v140, v141
	v_cvt_pk_bf16_f32 v141, v142, v143
	v_mov_b32_e32 v232, v144
	v_mov_b32_e32 v233, v145
	v_mov_b32_e32 v234, v140
	v_mov_b32_e32 v235, v141
	s_nop 1
	v_permlane16_swap_b32_e32 v232, v234
	v_permlane16_swap_b32_e32 v233, v235
	ds_bpermute_b32 v232, v244, v232
	ds_bpermute_b32 v233, v244, v233
	ds_bpermute_b32 v234, v244, v234
	ds_bpermute_b32 v235, v244, v235
	s_waitcnt lgkmcnt(4)
	global_store_dwordx4 v[182:183], v[228:231], off
	v_pk_mul_f32 v[136:137], v[174:175], v[136:137] op_sel_hi:[0,1]
	v_pk_mul_f32 v[138:139], v[174:175], v[138:139] op_sel_hi:[0,1]
	v_pk_mul_f32 v[142:143], v[68:69], v[132:133]
	v_pk_mul_f32 v[144:145], v[70:71], v[134:135]
	v_mad_i64_i32 v[140:141], s[34:35], v180, s36, v[176:177]
	v_pk_fma_f32 v[144:145], v[78:79], v[138:139], v[144:145] neg_lo:[0,0,1] neg_hi:[0,0,1]
	v_pk_fma_f32 v[142:143], v[76:77], v[136:137], v[142:143] neg_lo:[0,0,1] neg_hi:[0,0,1]
	v_pk_mul_f32 v[146:147], v[76:77], v[132:133]
	v_pk_mul_f32 v[180:181], v[78:79], v[134:135]
	v_lshl_add_u64 v[140:141], v[140:141], 0, v[178:179]
	v_pk_fma_f32 v[180:181], v[70:71], v[138:139], v[180:181]
	v_pk_fma_f32 v[146:147], v[68:69], v[136:137], v[146:147]
	v_cvt_pk_bf16_f32 v142, v142, v143
	v_cvt_pk_bf16_f32 v143, v144, v145
	v_lshlrev_b64 v[184:185], 7, v[168:169]
	v_cvt_pk_bf16_f32 v144, v146, v147
	v_cvt_pk_bf16_f32 v145, v180, v181
	v_mov_b32_e32 v236, v142
	v_mov_b32_e32 v237, v143
	v_mov_b32_e32 v238, v144
	v_mov_b32_e32 v239, v145
	s_nop 1
	v_permlane16_swap_b32_e32 v236, v238
	v_permlane16_swap_b32_e32 v237, v239
	ds_bpermute_b32 v236, v244, v236
	ds_bpermute_b32 v237, v244, v237
	ds_bpermute_b32 v238, v244, v238
	ds_bpermute_b32 v239, v244, v239
	s_waitcnt lgkmcnt(4)
; #define PG8_ST8(rs, b0, p, v) __builtin_amdgcn_raw_buffer_store_b64(v, rs, (int)((const char*)(p) - (const char*)(b0)), 0, 16)
; __device__ __forceinline__ unsigned cvt_pk_bf16(float lo, float hi) { unsigned r; asm volatile("v_cvt_pk_bf16_f32 %0, %1, %2" : "=v"(r) : "v"(lo), "v"(hi)); return r; }
;     __device__ __forceinline__ void operator()(const f32x4 (&acc)[2][2][4][2], const Unit& u, int wr, int wc, int fr, int fq) const {
;     ...
;             for (int ai = 0; ai < 2; ++ai) {
;                 f32x4 c4[4], s4[4];
; #pragma unroll
;                 for (int m = 0; m < 4; ++m) { const int row = row0 + ai * HALF + m * 16; c4[m] = *(const f32x4*)(rc + (size_t)row * 32 + f); s4[m] = *(const f32x4*)(rs + (size_t)row * 32 + f); }
;                 asm volatile("" ::: "memory");
; #pragma unroll
;                 for (int m = 0; m < 4; ++m) { const int row = row0 + ai * HALF + m * 16;
;                     const f32x4 cc = c4[m] * sc, ss = s4[m] * sc;
;                     bf16_t* rowp = P + (size_t)row * ldp + col0;
; #pragma unroll
;                     for (int bj = 0; bj < 2; ++bj) { const f32x4 x1 = acc[ai][bj][m][0], x2 = acc[ai][bj][m][1]; const f32x4 o1 = x1 * cc - x2 * ss, o2 = x2 * cc + x1 * ss;
;                         u32x2 w1, w2; w1.x = cvt_pk_bf16(o1[0], o1[1]); w1.y = cvt_pk_bf16(o1[2], o1[3]); w2.x = cvt_pk_bf16(o2[0], o2[1]); w2.y = cvt_pk_bf16(o2[2], o2[3]);
;                         PG8_ST8(rsp_, P, rowp + bj * HALF, w1); PG8_ST8(rsp_, P, rowp + bj * HALF + 32, w2); } }
	global_store_dwordx4 v[182:183], v[232:235], off offset:256
	v_pk_mul_f32 v[142:143], v[72:73], v[132:133]
	v_pk_mul_f32 v[144:145], v[74:75], v[134:135]
	v_pk_mul_f32 v[132:133], v[80:81], v[132:133]
	v_pk_fma_f32 v[144:145], v[82:83], v[138:139], v[144:145] neg_lo:[0,0,1] neg_hi:[0,0,1]
	v_pk_fma_f32 v[142:143], v[80:81], v[136:137], v[142:143] neg_lo:[0,0,1] neg_hi:[0,0,1]
	v_pk_mul_f32 v[134:135], v[82:83], v[134:135]
	v_pk_fma_f32 v[132:133], v[72:73], v[136:137], v[132:133]
	v_cvt_pk_bf16_f32 v136, v142, v143
	v_cvt_pk_bf16_f32 v137, v144, v145
	v_pk_fma_f32 v[134:135], v[74:75], v[138:139], v[134:135]
	v_cvt_pk_bf16_f32 v132, v132, v133
	v_lshlrev_b64 v[144:145], 7, v[170:171]
	v_cvt_pk_bf16_f32 v133, v134, v135
	v_mov_b32_e32 v240, v136
	v_mov_b32_e32 v241, v137
	v_mov_b32_e32 v242, v132
	v_mov_b32_e32 v243, v133
	s_nop 1
	v_permlane16_swap_b32_e32 v240, v242
	v_permlane16_swap_b32_e32 v241, v243
	ds_bpermute_b32 v240, v244, v240
	ds_bpermute_b32 v241, v244, v241
	ds_bpermute_b32 v242, v244, v242
	ds_bpermute_b32 v243, v244, v243
	s_waitcnt lgkmcnt(4)
	global_store_dwordx4 v[140:141], v[236:239], off
	s_waitcnt lgkmcnt(0)
	global_store_dwordx4 v[140:141], v[240:243], off offset:256
	v_lshlrev_b64 v[136:137], 7, v[172:173]
	v_lshl_add_u64 v[132:133], v[154:155], 0, v[136:137]
	v_lshl_add_u64 v[136:137], v[156:157], 0, v[136:137]
	global_load_dwordx4 v[132:135], v[132:133], off
	v_lshl_add_u64 v[140:141], v[154:155], 0, v[144:145]
	global_load_dwordx4 v[136:139], v[136:137], off
	v_lshl_add_u64 v[144:145], v[156:157], 0, v[144:145]
	global_load_dwordx4 v[140:143], v[140:141], off
	v_lshl_add_u64 v[180:181], v[154:155], 0, v[184:185]
	global_load_dwordx4 v[144:147], v[144:145], off
	v_lshl_add_u64 v[184:185], v[156:157], 0, v[184:185]
	global_load_dwordx4 v[180:183], v[180:181], off
	v_lshlrev_b64 v[192:193], 7, v[166:167]
	global_load_dwordx4 v[184:187], v[184:185], off
	v_lshl_add_u64 v[188:189], v[154:155], 0, v[192:193]
	v_lshl_add_u64 v[192:193], v[156:157], 0, v[192:193]
	global_load_dwordx4 v[188:191], v[188:189], off
	global_load_dwordx4 v[218:221], v[192:193], off
	s_waitcnt vmcnt(0)
	v_pk_mul_f32 v[132:133], v[174:175], v[132:133] op_sel_hi:[0,1]
	v_pk_mul_f32 v[138:139], v[174:175], v[138:139] op_sel_hi:[0,1]
	v_pk_mul_f32 v[136:137], v[174:175], v[136:137] op_sel_hi:[0,1]
	v_pk_mul_f32 v[134:135], v[174:175], v[134:135] op_sel_hi:[0,1]
	v_pk_mul_f32 v[198:199], v[52:53], v[136:137]
	v_pk_mul_f32 v[200:201], v[54:55], v[138:139]
	v_mad_i64_i32 v[206:207], s[34:35], v172, s36, v[176:177]
	v_pk_fma_f32 v[200:201], v[62:63], v[134:135], v[200:201] neg_lo:[0,0,1] neg_hi:[0,0,1]
	v_pk_fma_f32 v[198:199], v[60:61], v[132:133], v[198:199] neg_lo:[0,0,1] neg_hi:[0,0,1]
	v_pk_mul_f32 v[204:205], v[60:61], v[136:137]
	v_pk_mul_f32 v[208:209], v[62:63], v[138:139]
	v_lshl_add_u64 v[206:207], v[206:207], 0, v[178:179]
	v_pk_fma_f32 v[208:209], v[54:55], v[134:135], v[208:209]
	v_pk_fma_f32 v[204:205], v[52:53], v[132:133], v[204:205]
	v_cvt_pk_bf16_f32 v198, v198, v199
	v_cvt_pk_bf16_f32 v199, v200, v201
	s_nop 0
	v_cvt_pk_bf16_f32 v200, v204, v205
	v_cvt_pk_bf16_f32 v201, v208, v209
	v_mov_b32_e32 v228, v198
	v_mov_b32_e32 v229, v199
	v_mov_b32_e32 v230, v200
	v_mov_b32_e32 v231, v201
	s_nop 1
	v_permlane16_swap_b32_e32 v228, v230
	v_permlane16_swap_b32_e32 v229, v231
	ds_bpermute_b32 v228, v244, v228
	ds_bpermute_b32 v229, v244, v229
	ds_bpermute_b32 v230, v244, v230
	ds_bpermute_b32 v231, v244, v231
	v_pk_mul_f32 v[198:199], v[56:57], v[136:137]
	v_pk_mul_f32 v[200:201], v[58:59], v[138:139]
	v_pk_mul_f32 v[136:137], v[64:65], v[136:137]
	v_pk_fma_f32 v[200:201], v[66:67], v[134:135], v[200:201] neg_lo:[0,0,1] neg_hi:[0,0,1]
	v_pk_fma_f32 v[198:199], v[64:65], v[132:133], v[198:199] neg_lo:[0,0,1] neg_hi:[0,0,1]
	v_pk_mul_f32 v[138:139], v[66:67], v[138:139]
	v_pk_fma_f32 v[132:133], v[56:57], v[132:133], v[136:137]
	v_cvt_pk_bf16_f32 v136, v198, v199
	v_cvt_pk_bf16_f32 v137, v200, v201
	v_pk_fma_f32 v[134:135], v[58:59], v[134:135], v[138:139]
	v_cvt_pk_bf16_f32 v132, v132, v133
	v_pk_mul_f32 v[138:139], v[174:175], v[144:145] op_sel_hi:[0,1]
	v_cvt_pk_bf16_f32 v133, v134, v135
	v_mov_b32_e32 v232, v136
	v_mov_b32_e32 v233, v137
	v_mov_b32_e32 v234, v132
	v_mov_b32_e32 v235, v133
	s_nop 1
	v_permlane16_swap_b32_e32 v232, v234
	v_permlane16_swap_b32_e32 v233, v235
	ds_bpermute_b32 v232, v244, v232
	ds_bpermute_b32 v233, v244, v233
	ds_bpermute_b32 v234, v244, v234
	ds_bpermute_b32 v235, v244, v235
	s_waitcnt lgkmcnt(4)
	global_store_dwordx4 v[206:207], v[228:231], off
	v_pk_mul_f32 v[136:137], v[174:175], v[146:147] op_sel_hi:[0,1]
	v_pk_mul_f32 v[132:133], v[174:175], v[140:141] op_sel_hi:[0,1]
	v_pk_mul_f32 v[134:135], v[174:175], v[142:143] op_sel_hi:[0,1]
	v_pk_mul_f32 v[142:143], v[36:37], v[138:139]
	v_pk_mul_f32 v[144:145], v[38:39], v[136:137]
	v_mad_i64_i32 v[140:141], s[34:35], v170, s36, v[176:177]
	v_pk_fma_f32 v[144:145], v[46:47], v[134:135], v[144:145] neg_lo:[0,0,1] neg_hi:[0,0,1]
	v_pk_fma_f32 v[142:143], v[44:45], v[132:133], v[142:143] neg_lo:[0,0,1] neg_hi:[0,0,1]
	v_pk_mul_f32 v[146:147], v[44:45], v[138:139]
	v_pk_mul_f32 v[192:193], v[46:47], v[136:137]
	v_lshl_add_u64 v[140:141], v[140:141], 0, v[178:179]
	v_pk_fma_f32 v[192:193], v[38:39], v[134:135], v[192:193]
	v_pk_fma_f32 v[146:147], v[36:37], v[132:133], v[146:147]
	v_cvt_pk_bf16_f32 v142, v142, v143
	v_cvt_pk_bf16_f32 v143, v144, v145
	s_nop 0
	v_cvt_pk_bf16_f32 v144, v146, v147
	v_cvt_pk_bf16_f32 v145, v192, v193
	v_mov_b32_e32 v236, v142
	v_mov_b32_e32 v237, v143
	v_mov_b32_e32 v238, v144
	v_mov_b32_e32 v239, v145
	s_nop 1
	v_permlane16_swap_b32_e32 v236, v238
	v_permlane16_swap_b32_e32 v237, v239
	ds_bpermute_b32 v236, v244, v236
	ds_bpermute_b32 v237, v244, v237
	ds_bpermute_b32 v238, v244, v238
	ds_bpermute_b32 v239, v244, v239
	s_waitcnt lgkmcnt(4)
; #define PG8_ST8(rs, b0, p, v) __builtin_amdgcn_raw_buffer_store_b64(v, rs, (int)((const char*)(p) - (const char*)(b0)), 0, 16)
; __device__ __forceinline__ unsigned cvt_pk_bf16(float lo, float hi) { unsigned r; asm volatile("v_cvt_pk_bf16_f32 %0, %1, %2" : "=v"(r) : "v"(lo), "v"(hi)); return r; }
;     __device__ __forceinline__ void operator()(const f32x4 (&acc)[2][2][4][2], const Unit& u, int wr, int wc, int fr, int fq) const {
;     ...
;                 for (int m = 0; m < 4; ++m) { const int row = row0 + ai * HALF + m * 16;
;                     const f32x4 cc = c4[m] * sc, ss = s4[m] * sc;
;                     bf16_t* rowp = P + (size_t)row * ldp + col0;
; #pragma unroll
;                     for (int bj = 0; bj < 2; ++bj) { const f32x4 x1 = acc[ai][bj][m][0], x2 = acc[ai][bj][m][1]; const f32x4 o1 = x1 * cc - x2 * ss, o2 = x2 * cc + x1 * ss;
;                         u32x2 w1, w2; w1.x = cvt_pk_bf16(o1[0], o1[1]); w1.y = cvt_pk_bf16(o1[2], o1[3]); w2.x = cvt_pk_bf16(o2[0], o2[1]); w2.y = cvt_pk_bf16(o2[2], o2[3]);
;                         PG8_ST8(rsp_, P, rowp + bj * HALF, w1); PG8_ST8(rsp_, P, rowp + bj * HALF + 32, w2); } }
	global_store_dwordx4 v[206:207], v[232:235], off offset:256
	v_pk_mul_f32 v[142:143], v[40:41], v[138:139]
	v_pk_mul_f32 v[144:145], v[42:43], v[136:137]
	v_pk_mul_f32 v[138:139], v[48:49], v[138:139]
	v_pk_mul_f32 v[136:137], v[50:51], v[136:137]
	v_pk_fma_f32 v[144:145], v[50:51], v[134:135], v[144:145] neg_lo:[0,0,1] neg_hi:[0,0,1]
	v_pk_fma_f32 v[142:143], v[48:49], v[132:133], v[142:143] neg_lo:[0,0,1] neg_hi:[0,0,1]
	v_pk_fma_f32 v[134:135], v[42:43], v[134:135], v[136:137]
	v_pk_fma_f32 v[132:133], v[40:41], v[132:133], v[138:139]
	v_cvt_pk_bf16_f32 v136, v142, v143
	v_cvt_pk_bf16_f32 v137, v144, v145
	v_pk_mul_f32 v[138:139], v[174:175], v[184:185] op_sel_hi:[0,1]
	v_cvt_pk_bf16_f32 v132, v132, v133
	v_cvt_pk_bf16_f32 v133, v134, v135
	v_mov_b32_e32 v240, v136
	v_mov_b32_e32 v241, v137
	v_mov_b32_e32 v242, v132
	v_mov_b32_e32 v243, v133
	s_nop 1
	v_permlane16_swap_b32_e32 v240, v242
	v_permlane16_swap_b32_e32 v241, v243
	ds_bpermute_b32 v240, v244, v240
	ds_bpermute_b32 v241, v244, v241
	ds_bpermute_b32 v242, v244, v242
	ds_bpermute_b32 v243, v244, v243
	s_waitcnt lgkmcnt(4)
	global_store_dwordx4 v[140:141], v[236:239], off
	v_pk_mul_f32 v[136:137], v[174:175], v[186:187] op_sel_hi:[0,1]
	v_pk_mul_f32 v[132:133], v[174:175], v[180:181] op_sel_hi:[0,1]
	v_pk_mul_f32 v[134:135], v[174:175], v[182:183] op_sel_hi:[0,1]
	v_pk_mul_f32 v[142:143], v[20:21], v[138:139]
	v_pk_mul_f32 v[144:145], v[22:23], v[136:137]
	v_mad_i64_i32 v[206:207], s[34:35], v168, s36, v[176:177]
	v_pk_fma_f32 v[144:145], v[30:31], v[134:135], v[144:145] neg_lo:[0,0,1] neg_hi:[0,0,1]
	v_pk_fma_f32 v[142:143], v[28:29], v[132:133], v[142:143] neg_lo:[0,0,1] neg_hi:[0,0,1]
	v_pk_mul_f32 v[146:147], v[28:29], v[138:139]
	v_pk_mul_f32 v[180:181], v[30:31], v[136:137]
	v_lshl_add_u64 v[206:207], v[206:207], 0, v[178:179]
	v_pk_fma_f32 v[180:181], v[22:23], v[134:135], v[180:181]
	v_pk_fma_f32 v[146:147], v[20:21], v[132:133], v[146:147]
	v_cvt_pk_bf16_f32 v142, v142, v143
	v_cvt_pk_bf16_f32 v143, v144, v145
	s_nop 0
	v_cvt_pk_bf16_f32 v144, v146, v147
	v_cvt_pk_bf16_f32 v145, v180, v181
	v_mov_b32_e32 v228, v142
	v_mov_b32_e32 v229, v143
	v_mov_b32_e32 v230, v144
	v_mov_b32_e32 v231, v145
	s_nop 1
	v_permlane16_swap_b32_e32 v228, v230
	v_permlane16_swap_b32_e32 v229, v231
	ds_bpermute_b32 v228, v244, v228
	ds_bpermute_b32 v229, v244, v229
	ds_bpermute_b32 v230, v244, v230
	ds_bpermute_b32 v231, v244, v231
	s_waitcnt lgkmcnt(4)
	global_store_dwordx4 v[140:141], v[240:243], off offset:256
	v_pk_mul_f32 v[142:143], v[24:25], v[138:139]
	v_pk_mul_f32 v[144:145], v[26:27], v[136:137]
	v_pk_mul_f32 v[138:139], v[32:33], v[138:139]
	v_pk_mul_f32 v[136:137], v[34:35], v[136:137]
	v_pk_fma_f32 v[144:145], v[34:35], v[134:135], v[144:145] neg_lo:[0,0,1] neg_hi:[0,0,1]
	v_pk_fma_f32 v[142:143], v[32:33], v[132:133], v[142:143] neg_lo:[0,0,1] neg_hi:[0,0,1]
	v_pk_fma_f32 v[134:135], v[26:27], v[134:135], v[136:137]
	v_pk_fma_f32 v[132:133], v[24:25], v[132:133], v[138:139]
	v_cvt_pk_bf16_f32 v136, v142, v143
	v_cvt_pk_bf16_f32 v137, v144, v145
	v_pk_mul_f32 v[138:139], v[174:175], v[218:219] op_sel_hi:[0,1]
	v_cvt_pk_bf16_f32 v132, v132, v133
	v_cvt_pk_bf16_f32 v133, v134, v135
	v_mov_b32_e32 v232, v136
	v_mov_b32_e32 v233, v137
	v_mov_b32_e32 v234, v132
	v_mov_b32_e32 v235, v133
	s_nop 1
	v_permlane16_swap_b32_e32 v232, v234
	v_permlane16_swap_b32_e32 v233, v235
	ds_bpermute_b32 v232, v244, v232
	ds_bpermute_b32 v233, v244, v233
	ds_bpermute_b32 v234, v244, v234
	ds_bpermute_b32 v235, v244, v235
	s_waitcnt lgkmcnt(4)
	global_store_dwordx4 v[206:207], v[228:231], off
	v_pk_mul_f32 v[136:137], v[174:175], v[220:221] op_sel_hi:[0,1]
	v_pk_mul_f32 v[132:133], v[174:175], v[188:189] op_sel_hi:[0,1]
	v_pk_mul_f32 v[134:135], v[174:175], v[190:191] op_sel_hi:[0,1]
	v_pk_mul_f32 v[142:143], v[4:5], v[138:139]
	v_pk_mul_f32 v[144:145], v[6:7], v[136:137]
	v_mad_i64_i32 v[140:141], s[34:35], v166, s36, v[176:177]
	v_pk_fma_f32 v[144:145], v[14:15], v[134:135], v[144:145] neg_lo:[0,0,1] neg_hi:[0,0,1]
	v_pk_fma_f32 v[142:143], v[12:13], v[132:133], v[142:143] neg_lo:[0,0,1] neg_hi:[0,0,1]
	v_pk_mul_f32 v[146:147], v[12:13], v[138:139]
	v_pk_mul_f32 v[176:177], v[14:15], v[136:137]
	v_lshl_add_u64 v[140:141], v[140:141], 0, v[178:179]
	v_pk_fma_f32 v[176:177], v[6:7], v[134:135], v[176:177]
	v_pk_fma_f32 v[146:147], v[4:5], v[132:133], v[146:147]
	v_cvt_pk_bf16_f32 v142, v142, v143
	v_cvt_pk_bf16_f32 v143, v144, v145
	s_mov_b64 s[34:35], 0
	v_cvt_pk_bf16_f32 v144, v146, v147
	v_cvt_pk_bf16_f32 v145, v176, v177
	v_mov_b32_e32 v236, v142
	v_mov_b32_e32 v237, v143
	v_mov_b32_e32 v238, v144
	v_mov_b32_e32 v239, v145
	s_nop 1
	v_permlane16_swap_b32_e32 v236, v238
	v_permlane16_swap_b32_e32 v237, v239
	ds_bpermute_b32 v236, v244, v236
	ds_bpermute_b32 v237, v244, v237
	ds_bpermute_b32 v238, v244, v238
	ds_bpermute_b32 v239, v244, v239
	s_waitcnt lgkmcnt(4)
	global_store_dwordx4 v[206:207], v[232:235], off offset:256
	v_pk_mul_f32 v[142:143], v[8:9], v[138:139]
	v_pk_mul_f32 v[144:145], v[10:11], v[136:137]
	v_pk_mul_f32 v[138:139], v[16:17], v[138:139]
	v_pk_mul_f32 v[136:137], v[18:19], v[136:137]
	v_pk_fma_f32 v[144:145], v[18:19], v[134:135], v[144:145] neg_lo:[0,0,1] neg_hi:[0,0,1]
	v_pk_fma_f32 v[142:143], v[16:17], v[132:133], v[142:143] neg_lo:[0,0,1] neg_hi:[0,0,1]
	v_pk_fma_f32 v[134:135], v[10:11], v[134:135], v[136:137]
	v_pk_fma_f32 v[132:133], v[8:9], v[132:133], v[138:139]
	v_cvt_pk_bf16_f32 v136, v142, v143
	v_cvt_pk_bf16_f32 v137, v144, v145
	s_nop 0
	v_cvt_pk_bf16_f32 v132, v132, v133
	v_cvt_pk_bf16_f32 v133, v134, v135
	v_mov_b32_e32 v240, v136
	v_mov_b32_e32 v241, v137
	v_mov_b32_e32 v242, v132
	v_mov_b32_e32 v243, v133
	s_nop 1
	v_permlane16_swap_b32_e32 v240, v242
	v_permlane16_swap_b32_e32 v241, v243
	ds_bpermute_b32 v240, v244, v240
	ds_bpermute_b32 v241, v244, v241
	ds_bpermute_b32 v242, v244, v242
	ds_bpermute_b32 v243, v244, v243
	s_waitcnt lgkmcnt(4)
	global_store_dwordx4 v[140:141], v[236:239], off
	s_waitcnt lgkmcnt(0)
	global_store_dwordx4 v[140:141], v[240:243], off offset:256
